# in-projection unit loop: the wait for the epilogue stores moved behind the accumulator clearing
# baseline (speedup 1.0000x reference)
; #define PG8_GLOAD(v, slot_) do { const int _t = wid * 64 + lane_id_v(); _Pragma("unroll") for (int _i = 0; _i < 2; ++_i) { int _R, _C; stage_rc(_t * 16 + _i * 8192, _R, _C); \
;         _Pragma("unroll") for (int _h = 0; _h < 2; ++_h) { int _tk = gtok[(slot_) * 256 + 128 * _h + _R]; _tk = _tk < 0 ? 0 : _tk; v[_h][_i] = (unsigned)(_tk * K + _C) * 2u; } } } while (0)
; #define PG8_BAR __builtin_amdgcn_s_barrier()
; template <class Epi, class Sched, bool ALIGN_EPI, bool GATHER, bool F8 = false>
; __device__ __forceinline__ void gemm_phase(LAS unsigned char* lds, const Gemm g, const Sched& S, const Epi& E, const LAS int* gtok, const int tid) {
;     ...
;         const char* nA = GATHER ? cA : (has_next ? (const char*)g.A + (size_t)nxt.pm * tstep : cA); const char* nB = has_next ? (const char*)g.Bt + (size_t)nxt.pn * tstep : cB;
;     ...
; #pragma unroll
;         for (int a = 0; a < 2; ++a)
; #pragma unroll
;             for (int b = 0; b < 2; ++b)
; #pragma unroll
;                 for (int m = 0; m < 4; ++m)
; #pragma unroll
;                     for (int n = 0; n < 2; ++n) acc[a][b][m][n] = (f32x4){0.f, 0.f, 0.f, 0.f};
;         cur = nxt; cA = nA; cB = nB; ++ui;
;         if constexpr (GATHER) { PG8_GLOAD(vA, cur.slot); }
;         if constexpr (ALIGN_EPI) { if (wr == 1) PG8_BAR; }
.LBB0_124:
	s_ashr_i32 s71, s70, 31
	s_lshl_b64 s[72:73], s[70:71], 20
	s_add_u32 s72, s60, s72
	s_addc_u32 s73, s61, s73
	s_and_b64 s[74:75], s[0:1], exec
	s_cselect_b32 s71, s73, s79
	s_cselect_b32 s77, s72, s78
	s_ashr_i32 s69, s68, 31
	s_lshl_b64 s[74:75], s[68:69], 20
	s_add_u32 s74, s95, s74
	s_addc_u32 s75, s96, s75
	s_and_b64 s[82:83], s[0:1], exec
	s_cselect_b32 s69, s75, s81
	s_cselect_b32 vcc_lo, s74, s80
	s_add_u32 vcc_hi, s80, 0x100
	v_mov_b32_e32 v20, 0
	s_addc_u32 s33, s81, 0
	s_mov_b32 s56, -2
	v_mov_b32_e32 v21, v20
	v_mov_b32_e32 v22, v20
	v_mov_b32_e32 v23, v20
	v_mov_b32_e32 v32, v20
	v_mov_b32_e32 v33, v20
	v_mov_b32_e32 v34, v20
	v_mov_b32_e32 v35, v20
	v_mov_b32_e32 v48, v20
	v_mov_b32_e32 v49, v20
	v_mov_b32_e32 v50, v20
	v_mov_b32_e32 v51, v20
	v_mov_b32_e32 v56, v20
	v_mov_b32_e32 v57, v20
	v_mov_b32_e32 v58, v20
	v_mov_b32_e32 v59, v20
	v_mov_b32_e32 v0, v20
	v_mov_b32_e32 v1, v20
	v_mov_b32_e32 v2, v20
	v_mov_b32_e32 v3, v20
	v_mov_b32_e32 v4, v20
	v_mov_b32_e32 v5, v20
	v_mov_b32_e32 v6, v20
	v_mov_b32_e32 v7, v20
	v_mov_b32_e32 v8, v20
	v_mov_b32_e32 v9, v20
	v_mov_b32_e32 v10, v20
	v_mov_b32_e32 v11, v20
	v_mov_b32_e32 v12, v20
	v_mov_b32_e32 v13, v20
	v_mov_b32_e32 v14, v20
	v_mov_b32_e32 v15, v20
	v_mov_b32_e32 v28, v20
	v_mov_b32_e32 v29, v20
	v_mov_b32_e32 v30, v20
	v_mov_b32_e32 v31, v20
	v_mov_b32_e32 v40, v20
	v_mov_b32_e32 v41, v20
	v_mov_b32_e32 v42, v20
	v_mov_b32_e32 v43, v20
	v_mov_b32_e32 v52, v20
	v_mov_b32_e32 v53, v20
	v_mov_b32_e32 v54, v20
	v_mov_b32_e32 v55, v20
	v_mov_b32_e32 v60, v20
	v_mov_b32_e32 v61, v20
	v_mov_b32_e32 v62, v20
	v_mov_b32_e32 v63, v20
	v_mov_b32_e32 v64, v20
	v_mov_b32_e32 v65, v20
	v_mov_b32_e32 v66, v20
	v_mov_b32_e32 v67, v20
	v_mov_b32_e32 v72, v20
	v_mov_b32_e32 v73, v20
	v_mov_b32_e32 v74, v20
	v_mov_b32_e32 v75, v20
	v_mov_b32_e32 v80, v20
	v_mov_b32_e32 v81, v20
	v_mov_b32_e32 v82, v20
	v_mov_b32_e32 v83, v20
	v_mov_b32_e32 v88, v20
	v_mov_b32_e32 v89, v20
	v_mov_b32_e32 v90, v20
	v_mov_b32_e32 v91, v20
	v_mov_b32_e32 v96, v20
	v_mov_b32_e32 v97, v20
	v_mov_b32_e32 v98, v20
	v_mov_b32_e32 v99, v20
	v_mov_b32_e32 v104, v20
	v_mov_b32_e32 v105, v20
	v_mov_b32_e32 v106, v20
	v_mov_b32_e32 v107, v20
	v_mov_b32_e32 v112, v20
	v_mov_b32_e32 v113, v20
	v_mov_b32_e32 v114, v20
	v_mov_b32_e32 v115, v20
	v_mov_b32_e32 v120, v20
	v_mov_b32_e32 v121, v20
	v_mov_b32_e32 v122, v20
	v_mov_b32_e32 v123, v20
	v_mov_b32_e32 v68, v20
	v_mov_b32_e32 v69, v20
	v_mov_b32_e32 v70, v20
	v_mov_b32_e32 v71, v20
	v_mov_b32_e32 v76, v20
	v_mov_b32_e32 v77, v20
	v_mov_b32_e32 v78, v20
	v_mov_b32_e32 v79, v20
	v_mov_b32_e32 v84, v20
	v_mov_b32_e32 v85, v20
	v_mov_b32_e32 v86, v20
	v_mov_b32_e32 v87, v20
	v_mov_b32_e32 v92, v20
	v_mov_b32_e32 v93, v20
	v_mov_b32_e32 v94, v20
	v_mov_b32_e32 v95, v20
	v_mov_b32_e32 v100, v20
	v_mov_b32_e32 v101, v20
	v_mov_b32_e32 v102, v20
	v_mov_b32_e32 v103, v20
	v_mov_b32_e32 v108, v20
	v_mov_b32_e32 v109, v20
	v_mov_b32_e32 v110, v20
	v_mov_b32_e32 v111, v20
	v_mov_b32_e32 v116, v20
	v_mov_b32_e32 v117, v20
	v_mov_b32_e32 v118, v20
	v_mov_b32_e32 v119, v20
	v_mov_b32_e32 v124, v20
	v_mov_b32_e32 v125, v20
	v_mov_b32_e32 v126, v20
	v_mov_b32_e32 v127, v20
	v_mov_b32_e32 v44, v20
	v_mov_b32_e32 v45, v20
	v_mov_b32_e32 v46, v20
	v_mov_b32_e32 v47, v20
	v_mov_b32_e32 v36, v20
	v_mov_b32_e32 v37, v20
	v_mov_b32_e32 v38, v20
	v_mov_b32_e32 v39, v20
	v_mov_b32_e32 v24, v20
	v_mov_b32_e32 v25, v20
	v_mov_b32_e32 v26, v20
	v_mov_b32_e32 v27, v20
	v_mov_b32_e32 v16, v20
	v_mov_b32_e32 v17, v20
	v_mov_b32_e32 v18, v20
	v_mov_b32_e32 v19, v20
	s_waitcnt vmcnt(0)
